# speedup vs baseline: 1.0195x; 1.0045x over previous
.Lfp_tilestart:
	s_mov_b32 s33, s34
	s_mov_b32 s65, s38
	s_mov_b32 s37, s39
	v_mov_b32_e32 v166, v165
	s_cmp_ge_u32 s33, s32
	s_cbranch_scc1 .Lfp_exit
	v_mov_b32_e32 v66, 0
	v_mov_b32_e32 v67, 0
	v_mov_b32_e32 v68, 0
	v_mov_b32_e32 v69, 0
	v_mov_b32_e32 v70, 0
	v_mov_b32_e32 v71, 0
	v_mov_b32_e32 v72, 0
	v_mov_b32_e32 v73, 0
	v_mov_b32_e32 v74, 0
	v_mov_b32_e32 v75, 0
	v_mov_b32_e32 v76, 0
	v_mov_b32_e32 v77, 0
	v_mov_b32_e32 v78, 0
	v_mov_b32_e32 v79, 0
	v_mov_b32_e32 v80, 0
	v_mov_b32_e32 v81, 0
	v_lshlrev_b32_e32 v163, 2, v167
	v_add_u32_e32 v163, 0x24c00, v163
	ds_read_b32 v82, v163 offset:0
	ds_read_b32 v86, v163 offset:64
	ds_read_b32 v90, v163 offset:128
	ds_read_b32 v94, v163 offset:192
	ds_read_b32 v98, v163 offset:256
	ds_read_b32 v102, v163 offset:320
	ds_read_b32 v106, v163 offset:384
	ds_read_b32 v110, v163 offset:448
	s_waitcnt lgkmcnt(0)
	v_mov_b32_e32 v83, v82
	v_mov_b32_e32 v84, v82
	v_mov_b32_e32 v85, v82
	v_mov_b32_e32 v87, v86
	v_mov_b32_e32 v88, v86
	v_mov_b32_e32 v89, v86
	v_mov_b32_e32 v91, v90
	v_mov_b32_e32 v92, v90
	v_mov_b32_e32 v93, v90
	v_mov_b32_e32 v95, v94
	v_mov_b32_e32 v96, v94
	v_mov_b32_e32 v97, v94
	v_mov_b32_e32 v99, v98
	v_mov_b32_e32 v100, v98
	v_mov_b32_e32 v101, v98
	v_mov_b32_e32 v103, v102
	v_mov_b32_e32 v104, v102
	v_mov_b32_e32 v105, v102
	v_mov_b32_e32 v107, v106
	v_mov_b32_e32 v108, v106
	v_mov_b32_e32 v109, v106
	v_mov_b32_e32 v111, v110
	v_mov_b32_e32 v112, v110
	v_mov_b32_e32 v113, v110
	s_setprio 0
	s_cmp_eq_u32 s64, 3
	s_mov_b32 s64, 0
	s_cbranch_scc1 .Lfp_st_0
	s_cmp_eq_u32 s51, 0
	s_cbranch_scc1 .Lfp_is_0
	s_cmp_eq_u32 s51, 1
	s_cbranch_scc1 .Lfp_is_1
	s_cmp_eq_u32 s51, 2
	s_cbranch_scc1 .Lfp_is_2
	s_branch .Lfp_is_3

.Lfp_partend:
	s_setprio 2
	ds_write_b128 v136, v[66:69]
	ds_write_b128 v136, v[70:73] offset:64
	ds_write_b128 v136, v[74:77] offset:128
	ds_write_b128 v136, v[78:81] offset:192
	s_cmp_eq_u32 s66, 0
	s_cbranch_scc0 .Lfp_pe1
	ds_read_b128 v[126:129], v137
	ds_read_b128 v[114:117], v138
	ds_read_b128 v[118:121], v138 offset:1024
	ds_read_b128 v[122:125], v138 offset:2048
	ds_read_b128 v[66:69], v138 offset:3072
	ds_read_b128 v[70:73], v138 offset:4096
	ds_read_b128 v[74:77], v138 offset:5120
	ds_read_b128 v[78:81], v138 offset:6144
	s_waitcnt lgkmcnt(6)
	v_mfma_f32_16x16x32_f16 v[82:85], v[126:129], v[114:117], v[82:85]
	ds_read_b128 v[114:117], v138 offset:7168
	s_waitcnt lgkmcnt(6)
	v_mfma_f32_16x16x32_f16 v[86:89], v[126:129], v[118:121], v[86:89]
	ds_read_b128 v[130:133], v137 offset:64
	ds_read_b128 v[118:121], v138 offset:8192
	s_waitcnt lgkmcnt(7)
	v_mfma_f32_16x16x32_f16 v[90:93], v[126:129], v[122:125], v[90:93]
	ds_read_b128 v[122:125], v138 offset:9216
	s_waitcnt lgkmcnt(7)
	v_mfma_f32_16x16x32_f16 v[94:97], v[126:129], v[66:69], v[94:97]
	ds_read_b128 v[66:69], v138 offset:10240
	s_waitcnt lgkmcnt(7)
	v_mfma_f32_16x16x32_f16 v[98:101], v[126:129], v[70:73], v[98:101]
	ds_read_b128 v[70:73], v138 offset:11264
	s_waitcnt lgkmcnt(7)
	v_mfma_f32_16x16x32_f16 v[102:105], v[126:129], v[74:77], v[102:105]
	ds_read_b128 v[74:77], v138 offset:12288
	s_waitcnt lgkmcnt(7)
	v_mfma_f32_16x16x32_f16 v[106:109], v[126:129], v[78:81], v[106:109]
	ds_read_b128 v[78:81], v138 offset:13312
	s_waitcnt lgkmcnt(7)
	v_mfma_f32_16x16x32_f16 v[110:113], v[126:129], v[114:117], v[110:113]
	ds_read_b128 v[114:117], v138 offset:14336
	s_waitcnt lgkmcnt(6)
	v_mfma_f32_16x16x32_f16 v[82:85], v[130:133], v[118:121], v[82:85]
	ds_read_b128 v[118:121], v138 offset:15360
	s_waitcnt lgkmcnt(6)
	v_mfma_f32_16x16x32_f16 v[86:89], v[130:133], v[122:125], v[86:89]
	ds_read_b128 v[126:129], v137 offset:128
	ds_read_b128 v[122:125], v138 offset:16384
	s_waitcnt lgkmcnt(7)
	v_mfma_f32_16x16x32_f16 v[90:93], v[130:133], v[66:69], v[90:93]
	ds_read_b128 v[66:69], v138 offset:17408
	s_waitcnt lgkmcnt(7)
	v_mfma_f32_16x16x32_f16 v[94:97], v[130:133], v[70:73], v[94:97]
	ds_read_b128 v[70:73], v138 offset:18432
	s_waitcnt lgkmcnt(7)
	v_mfma_f32_16x16x32_f16 v[98:101], v[130:133], v[74:77], v[98:101]
	ds_read_b128 v[74:77], v138 offset:19456
	s_waitcnt lgkmcnt(7)
	v_mfma_f32_16x16x32_f16 v[102:105], v[130:133], v[78:81], v[102:105]
	ds_read_b128 v[78:81], v138 offset:20480
	s_waitcnt lgkmcnt(7)
	v_mfma_f32_16x16x32_f16 v[106:109], v[130:133], v[114:117], v[106:109]
	ds_read_b128 v[114:117], v138 offset:21504
	s_waitcnt lgkmcnt(7)
	v_mfma_f32_16x16x32_f16 v[110:113], v[130:133], v[118:121], v[110:113]
	ds_read_b128 v[118:121], v138 offset:22528
	s_waitcnt lgkmcnt(6)
	v_mfma_f32_16x16x32_f16 v[82:85], v[126:129], v[122:125], v[82:85]
	ds_read_b128 v[122:125], v138 offset:23552
	s_waitcnt lgkmcnt(6)
	v_mfma_f32_16x16x32_f16 v[86:89], v[126:129], v[66:69], v[86:89]
	ds_read_b128 v[130:133], v137 offset:192
	ds_read_b128 v[66:69], v138 offset:24576
	s_waitcnt lgkmcnt(7)
	v_mfma_f32_16x16x32_f16 v[90:93], v[126:129], v[70:73], v[90:93]
	ds_read_b128 v[70:73], v138 offset:25600
	s_waitcnt lgkmcnt(7)
	v_mfma_f32_16x16x32_f16 v[94:97], v[126:129], v[74:77], v[94:97]
	ds_read_b128 v[74:77], v138 offset:26624
	s_waitcnt lgkmcnt(7)
	v_mfma_f32_16x16x32_f16 v[98:101], v[126:129], v[78:81], v[98:101]
	ds_read_b128 v[78:81], v138 offset:27648
	s_waitcnt lgkmcnt(7)
	v_mfma_f32_16x16x32_f16 v[102:105], v[126:129], v[114:117], v[102:105]
	ds_read_b128 v[114:117], v138 offset:28672
	s_waitcnt lgkmcnt(7)
	v_mfma_f32_16x16x32_f16 v[106:109], v[126:129], v[118:121], v[106:109]
	ds_read_b128 v[118:121], v138 offset:29696
	s_waitcnt lgkmcnt(7)
	v_mfma_f32_16x16x32_f16 v[110:113], v[126:129], v[122:125], v[110:113]
	ds_read_b128 v[122:125], v138 offset:30720
	s_waitcnt lgkmcnt(6)
	v_mfma_f32_16x16x32_f16 v[82:85], v[130:133], v[66:69], v[82:85]
	ds_read_b128 v[66:69], v138 offset:31744
	s_waitcnt lgkmcnt(6)
	v_mfma_f32_16x16x32_f16 v[86:89], v[130:133], v[70:73], v[86:89]
	s_waitcnt lgkmcnt(5)
	v_mfma_f32_16x16x32_f16 v[90:93], v[130:133], v[74:77], v[90:93]
	s_waitcnt lgkmcnt(4)
	v_mfma_f32_16x16x32_f16 v[94:97], v[130:133], v[78:81], v[94:97]
	s_waitcnt lgkmcnt(3)
	v_mfma_f32_16x16x32_f16 v[98:101], v[130:133], v[114:117], v[98:101]
	s_waitcnt lgkmcnt(2)
	v_mfma_f32_16x16x32_f16 v[102:105], v[130:133], v[118:121], v[102:105]
	s_waitcnt lgkmcnt(1)
	v_mfma_f32_16x16x32_f16 v[106:109], v[130:133], v[122:125], v[106:109]
	s_waitcnt lgkmcnt(0)
	v_mfma_f32_16x16x32_f16 v[110:113], v[130:133], v[66:69], v[110:113]
	v_mov_b32_e32 v66, 0
	v_mov_b32_e32 v67, 0
	v_mov_b32_e32 v68, 0
	v_mov_b32_e32 v69, 0
	v_mov_b32_e32 v70, 0
	v_mov_b32_e32 v71, 0
	v_mov_b32_e32 v72, 0
	v_mov_b32_e32 v73, 0
	v_mov_b32_e32 v74, 0
	v_mov_b32_e32 v75, 0
	v_mov_b32_e32 v76, 0
	v_mov_b32_e32 v77, 0
	v_mov_b32_e32 v78, 0
	v_mov_b32_e32 v79, 0
	v_mov_b32_e32 v80, 0
	v_mov_b32_e32 v81, 0
	s_mov_b32 s66, 1
	s_mov_b32 s65, s37
	s_setprio 0
	s_cmp_eq_u32 s51, 0
	s_cbranch_scc1 .Lfp_is_0
	s_cmp_eq_u32 s51, 1
	s_cbranch_scc1 .Lfp_is_1
	s_cmp_eq_u32 s51, 2
	s_cbranch_scc1 .Lfp_is_2
	s_branch .Lfp_is_3
.Lfp_pe1:
	ds_read_b128 v[126:129], v137
	ds_read_b128 v[114:117], v138 offset:32768
	ds_read_b128 v[118:121], v138 offset:33792
	ds_read_b128 v[122:125], v138 offset:34816
	ds_read_b128 v[66:69], v138 offset:35840
	ds_read_b128 v[70:73], v138 offset:36864
	ds_read_b128 v[74:77], v138 offset:37888
	ds_read_b128 v[78:81], v138 offset:38912
	s_waitcnt lgkmcnt(6)
	v_mfma_f32_16x16x32_f16 v[82:85], v[126:129], v[114:117], v[82:85]
	ds_read_b128 v[114:117], v138 offset:39936
	s_waitcnt lgkmcnt(6)
	v_mfma_f32_16x16x32_f16 v[86:89], v[126:129], v[118:121], v[86:89]
	ds_read_b128 v[130:133], v137 offset:64
	ds_read_b128 v[118:121], v138 offset:40960
	s_waitcnt lgkmcnt(7)
	v_mfma_f32_16x16x32_f16 v[90:93], v[126:129], v[122:125], v[90:93]
	ds_read_b128 v[122:125], v138 offset:41984
	s_waitcnt lgkmcnt(7)
	v_mfma_f32_16x16x32_f16 v[94:97], v[126:129], v[66:69], v[94:97]
	ds_read_b128 v[66:69], v138 offset:43008
	s_waitcnt lgkmcnt(7)
	v_mfma_f32_16x16x32_f16 v[98:101], v[126:129], v[70:73], v[98:101]
	ds_read_b128 v[70:73], v138 offset:44032
	s_waitcnt lgkmcnt(7)
	v_mfma_f32_16x16x32_f16 v[102:105], v[126:129], v[74:77], v[102:105]
	ds_read_b128 v[74:77], v138 offset:45056
	s_waitcnt lgkmcnt(7)
	v_mfma_f32_16x16x32_f16 v[106:109], v[126:129], v[78:81], v[106:109]
	ds_read_b128 v[78:81], v138 offset:46080
	s_waitcnt lgkmcnt(7)
	v_mfma_f32_16x16x32_f16 v[110:113], v[126:129], v[114:117], v[110:113]
	ds_read_b128 v[114:117], v138 offset:47104
	s_waitcnt lgkmcnt(6)
	v_mfma_f32_16x16x32_f16 v[82:85], v[130:133], v[118:121], v[82:85]
	ds_read_b128 v[118:121], v138 offset:48128
	s_waitcnt lgkmcnt(6)
	v_mfma_f32_16x16x32_f16 v[86:89], v[130:133], v[122:125], v[86:89]
	ds_read_b128 v[126:129], v137 offset:128
	ds_read_b128 v[122:125], v138 offset:49152
	s_waitcnt lgkmcnt(7)
	v_mfma_f32_16x16x32_f16 v[90:93], v[130:133], v[66:69], v[90:93]
	ds_read_b128 v[66:69], v138 offset:50176
	s_waitcnt lgkmcnt(7)
	v_mfma_f32_16x16x32_f16 v[94:97], v[130:133], v[70:73], v[94:97]
	ds_read_b128 v[70:73], v138 offset:51200
	s_waitcnt lgkmcnt(7)
	v_mfma_f32_16x16x32_f16 v[98:101], v[130:133], v[74:77], v[98:101]
	ds_read_b128 v[74:77], v138 offset:52224
	s_waitcnt lgkmcnt(7)
	v_mfma_f32_16x16x32_f16 v[102:105], v[130:133], v[78:81], v[102:105]
	ds_read_b128 v[78:81], v138 offset:53248
	s_waitcnt lgkmcnt(7)
	v_mfma_f32_16x16x32_f16 v[106:109], v[130:133], v[114:117], v[106:109]
	ds_read_b128 v[114:117], v138 offset:54272
	s_waitcnt lgkmcnt(7)
	v_mfma_f32_16x16x32_f16 v[110:113], v[130:133], v[118:121], v[110:113]
	ds_read_b128 v[118:121], v138 offset:55296
	s_waitcnt lgkmcnt(6)
	v_mfma_f32_16x16x32_f16 v[82:85], v[126:129], v[122:125], v[82:85]
	ds_read_b128 v[122:125], v138 offset:56320
	s_waitcnt lgkmcnt(6)
	v_mfma_f32_16x16x32_f16 v[86:89], v[126:129], v[66:69], v[86:89]
	ds_read_b128 v[130:133], v137 offset:192
	ds_read_b128 v[66:69], v138 offset:57344
	s_waitcnt lgkmcnt(7)
	v_mfma_f32_16x16x32_f16 v[90:93], v[126:129], v[70:73], v[90:93]
	ds_read_b128 v[70:73], v138 offset:58368
	s_waitcnt lgkmcnt(7)
	v_mfma_f32_16x16x32_f16 v[94:97], v[126:129], v[74:77], v[94:97]
	ds_read_b128 v[74:77], v138 offset:59392
	s_waitcnt lgkmcnt(7)
	v_mfma_f32_16x16x32_f16 v[98:101], v[126:129], v[78:81], v[98:101]
	ds_read_b128 v[78:81], v138 offset:60416
	s_waitcnt lgkmcnt(7)
	v_mfma_f32_16x16x32_f16 v[102:105], v[126:129], v[114:117], v[102:105]
	ds_read_b128 v[114:117], v138 offset:61440
	s_waitcnt lgkmcnt(7)
	v_mfma_f32_16x16x32_f16 v[106:109], v[126:129], v[118:121], v[106:109]
	ds_read_b128 v[118:121], v138 offset:62464
	s_waitcnt lgkmcnt(7)
	v_mfma_f32_16x16x32_f16 v[110:113], v[126:129], v[122:125], v[110:113]
	ds_read_b128 v[122:125], v138 offset:63488
	s_waitcnt lgkmcnt(6)
	v_mfma_f32_16x16x32_f16 v[82:85], v[130:133], v[66:69], v[82:85]
	ds_read_b128 v[66:69], v138 offset:64512
	s_waitcnt lgkmcnt(6)
	v_mfma_f32_16x16x32_f16 v[86:89], v[130:133], v[70:73], v[86:89]
	s_waitcnt lgkmcnt(5)
	v_mfma_f32_16x16x32_f16 v[90:93], v[130:133], v[74:77], v[90:93]
	s_waitcnt lgkmcnt(4)
	v_mfma_f32_16x16x32_f16 v[94:97], v[130:133], v[78:81], v[94:97]
	s_waitcnt lgkmcnt(3)
	v_mfma_f32_16x16x32_f16 v[98:101], v[130:133], v[114:117], v[98:101]
	s_waitcnt lgkmcnt(2)
	v_mfma_f32_16x16x32_f16 v[102:105], v[130:133], v[118:121], v[102:105]
	s_waitcnt lgkmcnt(1)
	v_mfma_f32_16x16x32_f16 v[106:109], v[130:133], v[122:125], v[106:109]
	s_waitcnt lgkmcnt(0)
	v_mfma_f32_16x16x32_f16 v[110:113], v[130:133], v[66:69], v[110:113]
	s_mov_b32 s64, 1
	s_setprio 0
	s_cmp_eq_u32 s51, 0
	s_cbranch_scc1 .Lfp_is_0
	s_cmp_eq_u32 s51, 1
	s_cbranch_scc1 .Lfp_is_1
	s_cmp_eq_u32 s51, 2
	s_cbranch_scc1 .Lfp_is_2
	s_branch .Lfp_is_3
.Lfp_tileend:
	s_setprio 2
	ds_read_b128 v[126:129], v137
	ds_read_b128 v[114:117], v139
	ds_read_b128 v[118:121], v139 offset:1024
	ds_read_b128 v[122:125], v139 offset:2048
	ds_read_b128 v[66:69], v139 offset:3072
	ds_read_b128 v[70:73], v139 offset:4096
	ds_read_b128 v[74:77], v139 offset:5120
	ds_read_b128 v[78:81], v139 offset:6144
	s_waitcnt lgkmcnt(6)
	v_mfma_f32_16x16x32_f16 v[82:85], v[126:129], v[114:117], v[82:85]
	ds_read_b128 v[114:117], v139 offset:7168
	s_waitcnt lgkmcnt(6)
	v_mfma_f32_16x16x32_f16 v[86:89], v[126:129], v[118:121], v[86:89]
	ds_read_b128 v[130:133], v137 offset:64
	ds_read_b128 v[118:121], v139 offset:8192
	s_waitcnt lgkmcnt(7)
	v_mfma_f32_16x16x32_f16 v[90:93], v[126:129], v[122:125], v[90:93]
	ds_read_b128 v[122:125], v139 offset:9216
	s_waitcnt lgkmcnt(7)
	v_mfma_f32_16x16x32_f16 v[94:97], v[126:129], v[66:69], v[94:97]
	ds_read_b128 v[66:69], v139 offset:10240
	s_waitcnt lgkmcnt(7)
	v_mfma_f32_16x16x32_f16 v[98:101], v[126:129], v[70:73], v[98:101]
	ds_read_b128 v[70:73], v139 offset:11264
	s_waitcnt lgkmcnt(7)
	v_mfma_f32_16x16x32_f16 v[102:105], v[126:129], v[74:77], v[102:105]
	ds_read_b128 v[74:77], v139 offset:12288
	s_waitcnt lgkmcnt(7)
	v_mfma_f32_16x16x32_f16 v[106:109], v[126:129], v[78:81], v[106:109]
	ds_read_b128 v[78:81], v139 offset:13312
	s_waitcnt lgkmcnt(7)
	v_mfma_f32_16x16x32_f16 v[110:113], v[126:129], v[114:117], v[110:113]
	ds_read_b128 v[114:117], v139 offset:14336
	s_waitcnt lgkmcnt(6)
	v_mfma_f32_16x16x32_f16 v[82:85], v[130:133], v[118:121], v[82:85]
	ds_read_b128 v[118:121], v139 offset:15360
	s_waitcnt lgkmcnt(6)
	v_mfma_f32_16x16x32_f16 v[86:89], v[130:133], v[122:125], v[86:89]
	ds_read_b128 v[126:129], v137 offset:128
	ds_read_b128 v[122:125], v139 offset:16384
	s_waitcnt lgkmcnt(7)
	v_mfma_f32_16x16x32_f16 v[90:93], v[130:133], v[66:69], v[90:93]
	ds_read_b128 v[66:69], v139 offset:17408
	s_waitcnt lgkmcnt(7)
	v_mfma_f32_16x16x32_f16 v[94:97], v[130:133], v[70:73], v[94:97]
	ds_read_b128 v[70:73], v139 offset:18432
	s_waitcnt lgkmcnt(7)
	v_mfma_f32_16x16x32_f16 v[98:101], v[130:133], v[74:77], v[98:101]
	ds_read_b128 v[74:77], v139 offset:19456
	s_waitcnt lgkmcnt(7)
	v_mfma_f32_16x16x32_f16 v[102:105], v[130:133], v[78:81], v[102:105]
	ds_read_b128 v[78:81], v139 offset:20480
	s_waitcnt lgkmcnt(7)
	v_mfma_f32_16x16x32_f16 v[106:109], v[130:133], v[114:117], v[106:109]
	ds_read_b128 v[114:117], v139 offset:21504
	s_waitcnt lgkmcnt(7)
	v_mfma_f32_16x16x32_f16 v[110:113], v[130:133], v[118:121], v[110:113]
	ds_read_b128 v[118:121], v139 offset:22528
	s_waitcnt lgkmcnt(6)
	v_mfma_f32_16x16x32_f16 v[82:85], v[126:129], v[122:125], v[82:85]
	ds_read_b128 v[122:125], v139 offset:23552
	s_waitcnt lgkmcnt(6)
	v_mfma_f32_16x16x32_f16 v[86:89], v[126:129], v[66:69], v[86:89]
	ds_read_b128 v[130:133], v137 offset:192
	ds_read_b128 v[66:69], v139 offset:24576
	s_waitcnt lgkmcnt(7)
	v_mfma_f32_16x16x32_f16 v[90:93], v[126:129], v[70:73], v[90:93]
	ds_read_b128 v[70:73], v139 offset:25600
	s_waitcnt lgkmcnt(7)
	v_mfma_f32_16x16x32_f16 v[94:97], v[126:129], v[74:77], v[94:97]
	ds_read_b128 v[74:77], v139 offset:26624
	s_waitcnt lgkmcnt(7)
	v_mfma_f32_16x16x32_f16 v[98:101], v[126:129], v[78:81], v[98:101]
	ds_read_b128 v[78:81], v139 offset:27648
	s_waitcnt lgkmcnt(7)
	v_mfma_f32_16x16x32_f16 v[102:105], v[126:129], v[114:117], v[102:105]
	ds_read_b128 v[114:117], v139 offset:28672
	s_waitcnt lgkmcnt(7)
	v_mfma_f32_16x16x32_f16 v[106:109], v[126:129], v[118:121], v[106:109]
	ds_read_b128 v[118:121], v139 offset:29696
	s_waitcnt lgkmcnt(7)
	v_mfma_f32_16x16x32_f16 v[110:113], v[126:129], v[122:125], v[110:113]
	ds_read_b128 v[122:125], v139 offset:30720
	s_waitcnt lgkmcnt(6)
	v_mfma_f32_16x16x32_f16 v[82:85], v[130:133], v[66:69], v[82:85]
	ds_read_b128 v[66:69], v139 offset:31744
	s_waitcnt lgkmcnt(6)
	v_mfma_f32_16x16x32_f16 v[86:89], v[130:133], v[70:73], v[86:89]
	s_waitcnt lgkmcnt(5)
	v_mfma_f32_16x16x32_f16 v[90:93], v[130:133], v[74:77], v[90:93]
	s_waitcnt lgkmcnt(4)
	v_mfma_f32_16x16x32_f16 v[94:97], v[130:133], v[78:81], v[94:97]
	s_waitcnt lgkmcnt(3)
	v_mfma_f32_16x16x32_f16 v[98:101], v[130:133], v[114:117], v[98:101]
	s_waitcnt lgkmcnt(2)
	v_mfma_f32_16x16x32_f16 v[102:105], v[130:133], v[118:121], v[102:105]
	s_waitcnt lgkmcnt(1)
	v_mfma_f32_16x16x32_f16 v[106:109], v[130:133], v[122:125], v[106:109]
	s_waitcnt lgkmcnt(0)
	v_mfma_f32_16x16x32_f16 v[110:113], v[130:133], v[66:69], v[110:113]
	s_nop 7
	s_nop 3
	v_readlane_b32 s62, v166, 0
	v_readlane_b32 s63, v166, 15
	s_cmp_lg_u32 s62, s63
	s_cbranch_scc1 .Lfp_ep_nu
	v_max_f32_e32 v84, v84, v85
	v_max3_f32 v82, v82, v83, v84
	v_ashrrev_i32_e32 v83, 31, v82
	v_or_b32_e32 v83, 0x80000000, v83
	v_xor_b32_e32 v82, v82, v83
	v_max_f32_e32 v88, v88, v89
	v_max3_f32 v86, v86, v87, v88
	v_ashrrev_i32_e32 v87, 31, v86
	v_or_b32_e32 v87, 0x80000000, v87
	v_xor_b32_e32 v86, v86, v87
	v_max_f32_e32 v92, v92, v93
	v_max3_f32 v90, v90, v91, v92
	v_ashrrev_i32_e32 v91, 31, v90
	v_or_b32_e32 v91, 0x80000000, v91
	v_xor_b32_e32 v90, v90, v91
	v_max_f32_e32 v96, v96, v97
	v_max3_f32 v94, v94, v95, v96
	v_ashrrev_i32_e32 v95, 31, v94
	v_or_b32_e32 v95, 0x80000000, v95
	v_xor_b32_e32 v94, v94, v95
	v_max_f32_e32 v100, v100, v101
	v_max3_f32 v98, v98, v99, v100
	v_ashrrev_i32_e32 v99, 31, v98
	v_or_b32_e32 v99, 0x80000000, v99
	v_xor_b32_e32 v98, v98, v99
	v_max_f32_e32 v104, v104, v105
	v_max3_f32 v102, v102, v103, v104
	v_ashrrev_i32_e32 v103, 31, v102
	v_or_b32_e32 v103, 0x80000000, v103
	v_xor_b32_e32 v102, v102, v103
	v_max_f32_e32 v108, v108, v109
	v_max3_f32 v106, v106, v107, v108
	v_ashrrev_i32_e32 v107, 31, v106
	v_or_b32_e32 v107, 0x80000000, v107
	v_xor_b32_e32 v106, v106, v107
	v_max_f32_e32 v112, v112, v113
	v_max3_f32 v110, v110, v111, v112
	v_ashrrev_i32_e32 v111, 31, v110
	v_or_b32_e32 v111, 0x80000000, v111
	v_xor_b32_e32 v110, v110, v111
	s_sub_u32 s52, s62, s60
	s_cmp_lt_u32 s52, 8
	s_cbranch_scc0 .Lfp_ep_glob
	s_lshl_b32 s52, s52, 9
	s_add_u32 s52, s52, 0x24e00
	v_lshl_add_u32 v160, v167, 2, s52
	ds_max_u32 v160, v82
	ds_max_u32 v160, v86 offset:64
	ds_max_u32 v160, v90 offset:128
	ds_max_u32 v160, v94 offset:192
	ds_max_u32 v160, v98 offset:256
	ds_max_u32 v160, v102 offset:320
	ds_max_u32 v160, v106 offset:384
	ds_max_u32 v160, v110 offset:448
	s_branch .Lfp_ep_done

.Lfa_tilestart:
	s_mov_b32 s33, s34
	s_mov_b32 s65, s38
	s_mov_b32 s37, s39
	s_cmp_ge_u32 s33, s32
	s_cbranch_scc1 .Lfa_exit
	v_mov_b32_e32 v66, 0
	v_mov_b32_e32 v67, 0
	v_mov_b32_e32 v68, 0
	v_mov_b32_e32 v69, 0
	v_mov_b32_e32 v70, 0
	v_mov_b32_e32 v71, 0
	v_mov_b32_e32 v72, 0
	v_mov_b32_e32 v73, 0
	v_mov_b32_e32 v74, 0
	v_mov_b32_e32 v75, 0
	v_mov_b32_e32 v76, 0
	v_mov_b32_e32 v77, 0
	v_mov_b32_e32 v78, 0
	v_mov_b32_e32 v79, 0
	v_mov_b32_e32 v80, 0
	v_mov_b32_e32 v81, 0
	v_lshrrev_b32_e32 v163, 4, v159
	v_lshlrev_b32_e32 v163, 4, v163
	v_add_u32_e32 v163, 0x24c00, v163
	ds_read_b128 v[82:85], v163 offset:0
	ds_read_b128 v[86:89], v163 offset:64
	ds_read_b128 v[90:93], v163 offset:128
	ds_read_b128 v[94:97], v163 offset:192
	ds_read_b128 v[98:101], v163 offset:256
	ds_read_b128 v[102:105], v163 offset:320
	ds_read_b128 v[106:109], v163 offset:384
	ds_read_b128 v[110:113], v163 offset:448
	s_waitcnt lgkmcnt(0)
	s_setprio 0
	s_cmp_eq_u32 s64, 3
	s_mov_b32 s64, 0
	s_cbranch_scc1 .Lfa_st_0
	s_cmp_eq_u32 s51, 0
	s_cbranch_scc1 .Lfa_is_0
	s_cmp_eq_u32 s51, 1
	s_cbranch_scc1 .Lfa_is_1
	s_cmp_eq_u32 s51, 2
	s_cbranch_scc1 .Lfa_is_2
	s_branch .Lfa_is_3

.Lfa_partend:
	s_setprio 2
	ds_write_b128 v136, v[66:69]
	ds_write_b128 v136, v[70:73] offset:64
	ds_write_b128 v136, v[74:77] offset:128
	ds_write_b128 v136, v[78:81] offset:192
	s_cmp_eq_u32 s66, 0
	s_cbranch_scc0 .Lfa_pe1
	ds_read_b128 v[126:129], v137
	ds_read_b128 v[114:117], v138
	ds_read_b128 v[118:121], v138 offset:1024
	ds_read_b128 v[122:125], v138 offset:2048
	ds_read_b128 v[66:69], v138 offset:3072
	ds_read_b128 v[70:73], v138 offset:4096
	ds_read_b128 v[74:77], v138 offset:5120
	ds_read_b128 v[78:81], v138 offset:6144
	s_waitcnt lgkmcnt(6)
	v_mfma_f32_16x16x32_f16 v[82:85], v[114:117], v[126:129], v[82:85]
	ds_read_b128 v[114:117], v138 offset:7168
	s_waitcnt lgkmcnt(6)
	v_mfma_f32_16x16x32_f16 v[86:89], v[118:121], v[126:129], v[86:89]
	ds_read_b128 v[130:133], v137 offset:64
	ds_read_b128 v[118:121], v138 offset:8192
	s_waitcnt lgkmcnt(7)
	v_mfma_f32_16x16x32_f16 v[90:93], v[122:125], v[126:129], v[90:93]
	ds_read_b128 v[122:125], v138 offset:9216
	s_waitcnt lgkmcnt(7)
	v_mfma_f32_16x16x32_f16 v[94:97], v[66:69], v[126:129], v[94:97]
	ds_read_b128 v[66:69], v138 offset:10240
	s_waitcnt lgkmcnt(7)
	v_mfma_f32_16x16x32_f16 v[98:101], v[70:73], v[126:129], v[98:101]
	ds_read_b128 v[70:73], v138 offset:11264
	s_waitcnt lgkmcnt(7)
	v_mfma_f32_16x16x32_f16 v[102:105], v[74:77], v[126:129], v[102:105]
	ds_read_b128 v[74:77], v138 offset:12288
	s_waitcnt lgkmcnt(7)
	v_mfma_f32_16x16x32_f16 v[106:109], v[78:81], v[126:129], v[106:109]
	ds_read_b128 v[78:81], v138 offset:13312
	s_waitcnt lgkmcnt(7)
	v_mfma_f32_16x16x32_f16 v[110:113], v[114:117], v[126:129], v[110:113]
	ds_read_b128 v[114:117], v138 offset:14336
	s_waitcnt lgkmcnt(6)
	v_mfma_f32_16x16x32_f16 v[82:85], v[118:121], v[130:133], v[82:85]
	ds_read_b128 v[118:121], v138 offset:15360
	s_waitcnt lgkmcnt(6)
	v_mfma_f32_16x16x32_f16 v[86:89], v[122:125], v[130:133], v[86:89]
	ds_read_b128 v[126:129], v137 offset:128
	ds_read_b128 v[122:125], v138 offset:16384
	s_waitcnt lgkmcnt(7)
	v_mfma_f32_16x16x32_f16 v[90:93], v[66:69], v[130:133], v[90:93]
	ds_read_b128 v[66:69], v138 offset:17408
	s_waitcnt lgkmcnt(7)
	v_mfma_f32_16x16x32_f16 v[94:97], v[70:73], v[130:133], v[94:97]
	ds_read_b128 v[70:73], v138 offset:18432
	s_waitcnt lgkmcnt(7)
	v_mfma_f32_16x16x32_f16 v[98:101], v[74:77], v[130:133], v[98:101]
	ds_read_b128 v[74:77], v138 offset:19456
	s_waitcnt lgkmcnt(7)
	v_mfma_f32_16x16x32_f16 v[102:105], v[78:81], v[130:133], v[102:105]
	ds_read_b128 v[78:81], v138 offset:20480
	s_waitcnt lgkmcnt(7)
	v_mfma_f32_16x16x32_f16 v[106:109], v[114:117], v[130:133], v[106:109]
	ds_read_b128 v[114:117], v138 offset:21504
	s_waitcnt lgkmcnt(7)
	v_mfma_f32_16x16x32_f16 v[110:113], v[118:121], v[130:133], v[110:113]
	ds_read_b128 v[118:121], v138 offset:22528
	s_waitcnt lgkmcnt(6)
	v_mfma_f32_16x16x32_f16 v[82:85], v[122:125], v[126:129], v[82:85]
	ds_read_b128 v[122:125], v138 offset:23552
	s_waitcnt lgkmcnt(6)
	v_mfma_f32_16x16x32_f16 v[86:89], v[66:69], v[126:129], v[86:89]
	ds_read_b128 v[130:133], v137 offset:192
	ds_read_b128 v[66:69], v138 offset:24576
	s_waitcnt lgkmcnt(7)
	v_mfma_f32_16x16x32_f16 v[90:93], v[70:73], v[126:129], v[90:93]
	ds_read_b128 v[70:73], v138 offset:25600
	s_waitcnt lgkmcnt(7)
	v_mfma_f32_16x16x32_f16 v[94:97], v[74:77], v[126:129], v[94:97]
	ds_read_b128 v[74:77], v138 offset:26624
	s_waitcnt lgkmcnt(7)
	v_mfma_f32_16x16x32_f16 v[98:101], v[78:81], v[126:129], v[98:101]
	ds_read_b128 v[78:81], v138 offset:27648
	s_waitcnt lgkmcnt(7)
	v_mfma_f32_16x16x32_f16 v[102:105], v[114:117], v[126:129], v[102:105]
	ds_read_b128 v[114:117], v138 offset:28672
	s_waitcnt lgkmcnt(7)
	v_mfma_f32_16x16x32_f16 v[106:109], v[118:121], v[126:129], v[106:109]
	ds_read_b128 v[118:121], v138 offset:29696
	s_waitcnt lgkmcnt(7)
	v_mfma_f32_16x16x32_f16 v[110:113], v[122:125], v[126:129], v[110:113]
	ds_read_b128 v[122:125], v138 offset:30720
	s_waitcnt lgkmcnt(6)
	v_mfma_f32_16x16x32_f16 v[82:85], v[66:69], v[130:133], v[82:85]
	ds_read_b128 v[66:69], v138 offset:31744
	s_waitcnt lgkmcnt(6)
	v_mfma_f32_16x16x32_f16 v[86:89], v[70:73], v[130:133], v[86:89]
	s_waitcnt lgkmcnt(5)
	v_mfma_f32_16x16x32_f16 v[90:93], v[74:77], v[130:133], v[90:93]
	s_waitcnt lgkmcnt(4)
	v_mfma_f32_16x16x32_f16 v[94:97], v[78:81], v[130:133], v[94:97]
	s_waitcnt lgkmcnt(3)
	v_mfma_f32_16x16x32_f16 v[98:101], v[114:117], v[130:133], v[98:101]
	s_waitcnt lgkmcnt(2)
	v_mfma_f32_16x16x32_f16 v[102:105], v[118:121], v[130:133], v[102:105]
	s_waitcnt lgkmcnt(1)
	v_mfma_f32_16x16x32_f16 v[106:109], v[122:125], v[130:133], v[106:109]
	s_waitcnt lgkmcnt(0)
	v_mfma_f32_16x16x32_f16 v[110:113], v[66:69], v[130:133], v[110:113]
	v_mov_b32_e32 v66, 0
	v_mov_b32_e32 v67, 0
	v_mov_b32_e32 v68, 0
	v_mov_b32_e32 v69, 0
	v_mov_b32_e32 v70, 0
	v_mov_b32_e32 v71, 0
	v_mov_b32_e32 v72, 0
	v_mov_b32_e32 v73, 0
	v_mov_b32_e32 v74, 0
	v_mov_b32_e32 v75, 0
	v_mov_b32_e32 v76, 0
	v_mov_b32_e32 v77, 0
	v_mov_b32_e32 v78, 0
	v_mov_b32_e32 v79, 0
	v_mov_b32_e32 v80, 0
	v_mov_b32_e32 v81, 0
	s_mov_b32 s66, 1
	s_mov_b32 s65, s37
	s_setprio 0
	s_cmp_eq_u32 s51, 0
	s_cbranch_scc1 .Lfa_is_0
	s_cmp_eq_u32 s51, 1
	s_cbranch_scc1 .Lfa_is_1
	s_cmp_eq_u32 s51, 2
	s_cbranch_scc1 .Lfa_is_2
	s_branch .Lfa_is_3
.Lfa_pe1:
	ds_read_b128 v[126:129], v137
	ds_read_b128 v[114:117], v138 offset:32768
	ds_read_b128 v[118:121], v138 offset:33792
	ds_read_b128 v[122:125], v138 offset:34816
	ds_read_b128 v[66:69], v138 offset:35840
	ds_read_b128 v[70:73], v138 offset:36864
	ds_read_b128 v[74:77], v138 offset:37888
	ds_read_b128 v[78:81], v138 offset:38912
	s_waitcnt lgkmcnt(6)
	v_mfma_f32_16x16x32_f16 v[82:85], v[114:117], v[126:129], v[82:85]
	ds_read_b128 v[114:117], v138 offset:39936
	s_waitcnt lgkmcnt(6)
	v_mfma_f32_16x16x32_f16 v[86:89], v[118:121], v[126:129], v[86:89]
	ds_read_b128 v[130:133], v137 offset:64
	ds_read_b128 v[118:121], v138 offset:40960
	s_waitcnt lgkmcnt(7)
	v_mfma_f32_16x16x32_f16 v[90:93], v[122:125], v[126:129], v[90:93]
	ds_read_b128 v[122:125], v138 offset:41984
	s_waitcnt lgkmcnt(7)
	v_mfma_f32_16x16x32_f16 v[94:97], v[66:69], v[126:129], v[94:97]
	ds_read_b128 v[66:69], v138 offset:43008
	s_waitcnt lgkmcnt(7)
	v_mfma_f32_16x16x32_f16 v[98:101], v[70:73], v[126:129], v[98:101]
	ds_read_b128 v[70:73], v138 offset:44032
	s_waitcnt lgkmcnt(7)
	v_mfma_f32_16x16x32_f16 v[102:105], v[74:77], v[126:129], v[102:105]
	ds_read_b128 v[74:77], v138 offset:45056
	s_waitcnt lgkmcnt(7)
	v_mfma_f32_16x16x32_f16 v[106:109], v[78:81], v[126:129], v[106:109]
	ds_read_b128 v[78:81], v138 offset:46080
	s_waitcnt lgkmcnt(7)
	v_mfma_f32_16x16x32_f16 v[110:113], v[114:117], v[126:129], v[110:113]
	ds_read_b128 v[114:117], v138 offset:47104
	s_waitcnt lgkmcnt(6)
	v_mfma_f32_16x16x32_f16 v[82:85], v[118:121], v[130:133], v[82:85]
	ds_read_b128 v[118:121], v138 offset:48128
	s_waitcnt lgkmcnt(6)
	v_mfma_f32_16x16x32_f16 v[86:89], v[122:125], v[130:133], v[86:89]
	ds_read_b128 v[126:129], v137 offset:128
	ds_read_b128 v[122:125], v138 offset:49152
	s_waitcnt lgkmcnt(7)
	v_mfma_f32_16x16x32_f16 v[90:93], v[66:69], v[130:133], v[90:93]
	ds_read_b128 v[66:69], v138 offset:50176
	s_waitcnt lgkmcnt(7)
	v_mfma_f32_16x16x32_f16 v[94:97], v[70:73], v[130:133], v[94:97]
	ds_read_b128 v[70:73], v138 offset:51200
	s_waitcnt lgkmcnt(7)
	v_mfma_f32_16x16x32_f16 v[98:101], v[74:77], v[130:133], v[98:101]
	ds_read_b128 v[74:77], v138 offset:52224
	s_waitcnt lgkmcnt(7)
	v_mfma_f32_16x16x32_f16 v[102:105], v[78:81], v[130:133], v[102:105]
	ds_read_b128 v[78:81], v138 offset:53248
	s_waitcnt lgkmcnt(7)
	v_mfma_f32_16x16x32_f16 v[106:109], v[114:117], v[130:133], v[106:109]
	ds_read_b128 v[114:117], v138 offset:54272
	s_waitcnt lgkmcnt(7)
	v_mfma_f32_16x16x32_f16 v[110:113], v[118:121], v[130:133], v[110:113]
	ds_read_b128 v[118:121], v138 offset:55296
	s_waitcnt lgkmcnt(6)
	v_mfma_f32_16x16x32_f16 v[82:85], v[122:125], v[126:129], v[82:85]
	ds_read_b128 v[122:125], v138 offset:56320
	s_waitcnt lgkmcnt(6)
	v_mfma_f32_16x16x32_f16 v[86:89], v[66:69], v[126:129], v[86:89]
	s_waitcnt lgkmcnt(5)
	v_mfma_f32_16x16x32_f16 v[90:93], v[70:73], v[126:129], v[90:93]
	s_waitcnt lgkmcnt(4)
	v_mfma_f32_16x16x32_f16 v[94:97], v[74:77], v[126:129], v[94:97]
	s_waitcnt lgkmcnt(3)
	v_mfma_f32_16x16x32_f16 v[98:101], v[78:81], v[126:129], v[98:101]
	s_waitcnt lgkmcnt(2)
	v_mfma_f32_16x16x32_f16 v[102:105], v[114:117], v[126:129], v[102:105]
	s_waitcnt lgkmcnt(1)
	v_mfma_f32_16x16x32_f16 v[106:109], v[118:121], v[126:129], v[106:109]
	s_waitcnt lgkmcnt(0)
	v_mfma_f32_16x16x32_f16 v[110:113], v[122:125], v[126:129], v[110:113]
	s_mov_b32 s64, 1
	s_setprio 0
	s_cmp_eq_u32 s51, 0
	s_cbranch_scc1 .Lfa_is_0
	s_cmp_eq_u32 s51, 1
	s_cbranch_scc1 .Lfa_is_1
	s_cmp_eq_u32 s51, 2
	s_cbranch_scc1 .Lfa_is_2
	s_branch .Lfa_is_3
.Lfa_tileend:
	s_setprio 2
	ds_read_b128 v[126:129], v137
	ds_read_b128 v[114:117], v138 offset:57344
	ds_read_b128 v[118:121], v138 offset:58368
	ds_read_b128 v[122:125], v138 offset:59392
	ds_read_b128 v[66:69], v138 offset:60416
	ds_read_b128 v[70:73], v138 offset:61440
	ds_read_b128 v[74:77], v138 offset:62464
	ds_read_b128 v[78:81], v138 offset:63488
	s_waitcnt lgkmcnt(6)
	v_mfma_f32_16x16x32_f16 v[82:85], v[114:117], v[126:129], v[82:85]
	ds_read_b128 v[114:117], v138 offset:64512
	s_waitcnt lgkmcnt(6)
	v_mfma_f32_16x16x32_f16 v[86:89], v[118:121], v[126:129], v[86:89]
	ds_read_b128 v[130:133], v137 offset:64
	ds_read_b128 v[118:121], v139
	s_waitcnt lgkmcnt(7)
	v_mfma_f32_16x16x32_f16 v[90:93], v[122:125], v[126:129], v[90:93]
	ds_read_b128 v[122:125], v139 offset:1024
	s_waitcnt lgkmcnt(7)
	v_mfma_f32_16x16x32_f16 v[94:97], v[66:69], v[126:129], v[94:97]
	ds_read_b128 v[66:69], v139 offset:2048
	s_waitcnt lgkmcnt(7)
	v_mfma_f32_16x16x32_f16 v[98:101], v[70:73], v[126:129], v[98:101]
	ds_read_b128 v[70:73], v139 offset:3072
	s_waitcnt lgkmcnt(7)
	v_mfma_f32_16x16x32_f16 v[102:105], v[74:77], v[126:129], v[102:105]
	ds_read_b128 v[74:77], v139 offset:4096
	s_waitcnt lgkmcnt(7)
	v_mfma_f32_16x16x32_f16 v[106:109], v[78:81], v[126:129], v[106:109]
	ds_read_b128 v[78:81], v139 offset:5120
	s_waitcnt lgkmcnt(7)
	v_mfma_f32_16x16x32_f16 v[110:113], v[114:117], v[126:129], v[110:113]
	ds_read_b128 v[114:117], v139 offset:6144
	s_waitcnt lgkmcnt(6)
	v_mfma_f32_16x16x32_f16 v[82:85], v[118:121], v[130:133], v[82:85]
	ds_read_b128 v[118:121], v139 offset:7168
	s_waitcnt lgkmcnt(6)
	v_mfma_f32_16x16x32_f16 v[86:89], v[122:125], v[130:133], v[86:89]
	ds_read_b128 v[126:129], v137 offset:128
	ds_read_b128 v[122:125], v139 offset:8192
	s_waitcnt lgkmcnt(7)
	v_mfma_f32_16x16x32_f16 v[90:93], v[66:69], v[130:133], v[90:93]
	ds_read_b128 v[66:69], v139 offset:9216
	s_waitcnt lgkmcnt(7)
	v_mfma_f32_16x16x32_f16 v[94:97], v[70:73], v[130:133], v[94:97]
	ds_read_b128 v[70:73], v139 offset:10240
	s_waitcnt lgkmcnt(7)
	v_mfma_f32_16x16x32_f16 v[98:101], v[74:77], v[130:133], v[98:101]
	ds_read_b128 v[74:77], v139 offset:11264
	s_waitcnt lgkmcnt(7)
	v_mfma_f32_16x16x32_f16 v[102:105], v[78:81], v[130:133], v[102:105]
	ds_read_b128 v[78:81], v139 offset:12288
	s_waitcnt lgkmcnt(7)
	v_mfma_f32_16x16x32_f16 v[106:109], v[114:117], v[130:133], v[106:109]
	ds_read_b128 v[114:117], v139 offset:13312
	s_waitcnt lgkmcnt(7)
	v_mfma_f32_16x16x32_f16 v[110:113], v[118:121], v[130:133], v[110:113]
	ds_read_b128 v[118:121], v139 offset:14336
	s_waitcnt lgkmcnt(6)
	v_mfma_f32_16x16x32_f16 v[82:85], v[122:125], v[126:129], v[82:85]
	ds_read_b128 v[122:125], v139 offset:15360
	s_waitcnt lgkmcnt(6)
	v_mfma_f32_16x16x32_f16 v[86:89], v[66:69], v[126:129], v[86:89]
	s_waitcnt lgkmcnt(5)
	v_mfma_f32_16x16x32_f16 v[90:93], v[70:73], v[126:129], v[90:93]
	s_waitcnt lgkmcnt(4)
	v_mfma_f32_16x16x32_f16 v[94:97], v[74:77], v[126:129], v[94:97]
	s_waitcnt lgkmcnt(3)
	v_mfma_f32_16x16x32_f16 v[98:101], v[78:81], v[126:129], v[98:101]
	s_waitcnt lgkmcnt(2)
	v_mfma_f32_16x16x32_f16 v[102:105], v[114:117], v[126:129], v[102:105]
	s_waitcnt lgkmcnt(1)
	v_mfma_f32_16x16x32_f16 v[106:109], v[118:121], v[126:129], v[106:109]
	s_waitcnt lgkmcnt(0)
	v_mfma_f32_16x16x32_f16 v[110:113], v[122:125], v[126:129], v[110:113]
	s_nop 7
	s_nop 3
	v_max_f32_e32 v82, 0, v82
	v_max_f32_e32 v83, 0, v83
	v_max_f32_e32 v84, 0, v84
	v_max_f32_e32 v85, 0, v85
	v_cvt_pk_f16_f32 v160, v82, v83
	v_cvt_pk_f16_f32 v161, v84, v85
	ds_write_b64 v140, v[160:161]
	v_max_f32_e32 v86, 0, v86
	v_max_f32_e32 v87, 0, v87
	v_max_f32_e32 v88, 0, v88
	v_max_f32_e32 v89, 0, v89
	v_cvt_pk_f16_f32 v162, v86, v87
	v_cvt_pk_f16_f32 v163, v88, v89
	ds_write_b64 v140, v[162:163] offset:32
	v_max_f32_e32 v90, 0, v90
	v_max_f32_e32 v91, 0, v91
	v_max_f32_e32 v92, 0, v92
	v_max_f32_e32 v93, 0, v93
	v_cvt_pk_f16_f32 v160, v90, v91
	v_cvt_pk_f16_f32 v161, v92, v93
	ds_write_b64 v140, v[160:161] offset:64
	v_max_f32_e32 v94, 0, v94
	v_max_f32_e32 v95, 0, v95
	v_max_f32_e32 v96, 0, v96
	v_max_f32_e32 v97, 0, v97
	v_cvt_pk_f16_f32 v162, v94, v95
	v_cvt_pk_f16_f32 v163, v96, v97
	ds_write_b64 v140, v[162:163] offset:96
	v_max_f32_e32 v98, 0, v98
	v_max_f32_e32 v99, 0, v99
	v_max_f32_e32 v100, 0, v100
	v_max_f32_e32 v101, 0, v101
	v_cvt_pk_f16_f32 v160, v98, v99
	v_cvt_pk_f16_f32 v161, v100, v101
	ds_write_b64 v140, v[160:161] offset:128
	v_max_f32_e32 v102, 0, v102
	v_max_f32_e32 v103, 0, v103
	v_max_f32_e32 v104, 0, v104
	v_max_f32_e32 v105, 0, v105
	v_cvt_pk_f16_f32 v162, v102, v103
	v_cvt_pk_f16_f32 v163, v104, v105
	ds_write_b64 v140, v[162:163] offset:160
	v_max_f32_e32 v106, 0, v106
	v_max_f32_e32 v107, 0, v107
	v_max_f32_e32 v108, 0, v108
	v_max_f32_e32 v109, 0, v109
	v_cvt_pk_f16_f32 v160, v106, v107
	v_cvt_pk_f16_f32 v161, v108, v109
	ds_write_b64 v140, v[160:161] offset:192
	v_max_f32_e32 v110, 0, v110
	v_max_f32_e32 v111, 0, v111
	v_max_f32_e32 v112, 0, v112
	v_max_f32_e32 v113, 0, v113
	v_cvt_pk_f16_f32 v162, v110, v111
	v_cvt_pk_f16_f32 v163, v112, v113
	ds_write_b64 v140, v[162:163] offset:224
	s_lshl_b32 s52, s33, 12
	v_add_u32_e32 v158, s52, v142
	ds_read_b128 v[114:117], v141
	ds_read_b128 v[118:121], v141 offset:1088
	ds_read_b128 v[122:125], v141 offset:2176
	ds_read_b128 v[126:129], v141 offset:3264
	s_waitcnt lgkmcnt(3)
	global_store_dwordx4 v158, v[114:117], s[22:23] sc1
	s_waitcnt lgkmcnt(2)
	global_store_dwordx4 v158, v[118:121], s[22:23] offset:1024 sc1
	s_waitcnt lgkmcnt(1)
	global_store_dwordx4 v158, v[122:125], s[22:23] offset:2048 sc1
	s_waitcnt lgkmcnt(0)
	global_store_dwordx4 v158, v[126:129], s[22:23] offset:3072 sc1
	s_nop 1
	s_mov_b32 s66, 0
	s_branch .Lfa_tilestart

.Lfb_pe1:
	ds_read_b128 v[126:129], v137
	ds_read_b128 v[114:117], v138 offset:32768
	ds_read_b128 v[118:121], v138 offset:33792
	ds_read_b128 v[122:125], v138 offset:34816
	ds_read_b128 v[66:69], v138 offset:35840
	ds_read_b128 v[70:73], v138 offset:36864
	ds_read_b128 v[74:77], v138 offset:37888
	ds_read_b128 v[78:81], v138 offset:38912
	s_waitcnt lgkmcnt(6)
	v_mfma_f32_16x16x32_f16 v[82:85], v[114:117], v[126:129], v[82:85]
	ds_read_b128 v[114:117], v138 offset:39936
	s_waitcnt lgkmcnt(6)
	v_mfma_f32_16x16x32_f16 v[86:89], v[118:121], v[126:129], v[86:89]
	ds_read_b128 v[130:133], v137 offset:64
	ds_read_b128 v[118:121], v138 offset:40960
	s_waitcnt lgkmcnt(7)
	v_mfma_f32_16x16x32_f16 v[90:93], v[122:125], v[126:129], v[90:93]
	ds_read_b128 v[122:125], v138 offset:41984
	s_waitcnt lgkmcnt(7)
	v_mfma_f32_16x16x32_f16 v[94:97], v[66:69], v[126:129], v[94:97]
	ds_read_b128 v[66:69], v138 offset:43008
	s_waitcnt lgkmcnt(7)
	v_mfma_f32_16x16x32_f16 v[98:101], v[70:73], v[126:129], v[98:101]
	ds_read_b128 v[70:73], v138 offset:44032
	s_waitcnt lgkmcnt(7)
	v_mfma_f32_16x16x32_f16 v[102:105], v[74:77], v[126:129], v[102:105]
	ds_read_b128 v[74:77], v138 offset:45056
	s_waitcnt lgkmcnt(7)
	v_mfma_f32_16x16x32_f16 v[106:109], v[78:81], v[126:129], v[106:109]
	ds_read_b128 v[78:81], v138 offset:46080
	s_waitcnt lgkmcnt(7)
	v_mfma_f32_16x16x32_f16 v[110:113], v[114:117], v[126:129], v[110:113]
	ds_read_b128 v[114:117], v138 offset:47104
	s_waitcnt lgkmcnt(6)
	v_mfma_f32_16x16x32_f16 v[82:85], v[118:121], v[130:133], v[82:85]
	ds_read_b128 v[118:121], v138 offset:48128
	s_waitcnt lgkmcnt(6)
	v_mfma_f32_16x16x32_f16 v[86:89], v[122:125], v[130:133], v[86:89]
	ds_read_b128 v[126:129], v137 offset:128
	ds_read_b128 v[122:125], v138 offset:49152
	s_waitcnt lgkmcnt(7)
	v_mfma_f32_16x16x32_f16 v[90:93], v[66:69], v[130:133], v[90:93]
	ds_read_b128 v[66:69], v138 offset:50176
	s_waitcnt lgkmcnt(7)
	v_mfma_f32_16x16x32_f16 v[94:97], v[70:73], v[130:133], v[94:97]
	ds_read_b128 v[70:73], v138 offset:51200
	s_waitcnt lgkmcnt(7)
	v_mfma_f32_16x16x32_f16 v[98:101], v[74:77], v[130:133], v[98:101]
	ds_read_b128 v[74:77], v138 offset:52224
	s_waitcnt lgkmcnt(7)
	v_mfma_f32_16x16x32_f16 v[102:105], v[78:81], v[130:133], v[102:105]
	ds_read_b128 v[78:81], v138 offset:53248
	s_waitcnt lgkmcnt(7)
	v_mfma_f32_16x16x32_f16 v[106:109], v[114:117], v[130:133], v[106:109]
	ds_read_b128 v[114:117], v138 offset:54272
	s_waitcnt lgkmcnt(7)
	v_mfma_f32_16x16x32_f16 v[110:113], v[118:121], v[130:133], v[110:113]
	ds_read_b128 v[118:121], v138 offset:55296
	s_waitcnt lgkmcnt(6)
	v_mfma_f32_16x16x32_f16 v[82:85], v[122:125], v[126:129], v[82:85]
	ds_read_b128 v[122:125], v138 offset:56320
	s_waitcnt lgkmcnt(6)
	v_mfma_f32_16x16x32_f16 v[86:89], v[66:69], v[126:129], v[86:89]
	ds_read_b128 v[130:133], v137 offset:192
	ds_read_b128 v[66:69], v138 offset:57344
	s_waitcnt lgkmcnt(7)
	v_mfma_f32_16x16x32_f16 v[90:93], v[70:73], v[126:129], v[90:93]
	ds_read_b128 v[70:73], v138 offset:58368
	s_waitcnt lgkmcnt(7)
	v_mfma_f32_16x16x32_f16 v[94:97], v[74:77], v[126:129], v[94:97]
	ds_read_b128 v[74:77], v138 offset:59392
	s_waitcnt lgkmcnt(7)
	v_mfma_f32_16x16x32_f16 v[98:101], v[78:81], v[126:129], v[98:101]
	ds_read_b128 v[78:81], v138 offset:60416
	s_waitcnt lgkmcnt(7)
	v_mfma_f32_16x16x32_f16 v[102:105], v[114:117], v[126:129], v[102:105]
	ds_read_b128 v[114:117], v138 offset:61440
	s_waitcnt lgkmcnt(7)
	v_mfma_f32_16x16x32_f16 v[106:109], v[118:121], v[126:129], v[106:109]
	ds_read_b128 v[118:121], v138 offset:62464
	s_waitcnt lgkmcnt(7)
	v_mfma_f32_16x16x32_f16 v[110:113], v[122:125], v[126:129], v[110:113]
	ds_read_b128 v[122:125], v138 offset:63488
	s_waitcnt lgkmcnt(6)
	v_mfma_f32_16x16x32_f16 v[82:85], v[66:69], v[130:133], v[82:85]
	ds_read_b128 v[66:69], v138 offset:64512
	s_waitcnt lgkmcnt(6)
	v_mfma_f32_16x16x32_f16 v[86:89], v[70:73], v[130:133], v[86:89]
	s_waitcnt lgkmcnt(5)
	v_mfma_f32_16x16x32_f16 v[90:93], v[74:77], v[130:133], v[90:93]
	s_waitcnt lgkmcnt(4)
	v_mfma_f32_16x16x32_f16 v[94:97], v[78:81], v[130:133], v[94:97]
	s_waitcnt lgkmcnt(3)
	v_mfma_f32_16x16x32_f16 v[98:101], v[114:117], v[130:133], v[98:101]
	s_waitcnt lgkmcnt(2)
	v_mfma_f32_16x16x32_f16 v[102:105], v[118:121], v[130:133], v[102:105]
	s_waitcnt lgkmcnt(1)
	v_mfma_f32_16x16x32_f16 v[106:109], v[122:125], v[130:133], v[106:109]
	s_waitcnt lgkmcnt(0)
	v_mfma_f32_16x16x32_f16 v[110:113], v[66:69], v[130:133], v[110:113]
	s_mov_b32 s64, 1
	s_setprio 0
	s_cmp_eq_u32 s51, 0
	s_cbranch_scc1 .Lfb_is_0
	s_cmp_eq_u32 s51, 1
	s_cbranch_scc1 .Lfb_is_1
	s_cmp_eq_u32 s51, 2
	s_cbranch_scc1 .Lfb_is_2
	s_branch .Lfb_is_3
.Lfb_tileend:
	s_setprio 2
	ds_read_b128 v[126:129], v137
	ds_read_b128 v[114:117], v139
	ds_read_b128 v[118:121], v139 offset:1024
	ds_read_b128 v[122:125], v139 offset:2048
	ds_read_b128 v[66:69], v139 offset:3072
	ds_read_b128 v[70:73], v139 offset:4096
	ds_read_b128 v[74:77], v139 offset:5120
	ds_read_b128 v[78:81], v139 offset:6144
	s_waitcnt lgkmcnt(6)
	v_mfma_f32_16x16x32_f16 v[82:85], v[114:117], v[126:129], v[82:85]
	ds_read_b128 v[114:117], v139 offset:7168
	s_waitcnt lgkmcnt(6)
	v_mfma_f32_16x16x32_f16 v[86:89], v[118:121], v[126:129], v[86:89]
	ds_read_b128 v[130:133], v137 offset:64
	ds_read_b128 v[118:121], v139 offset:8192
	s_waitcnt lgkmcnt(7)
	v_mfma_f32_16x16x32_f16 v[90:93], v[122:125], v[126:129], v[90:93]
	ds_read_b128 v[122:125], v139 offset:9216
	s_waitcnt lgkmcnt(7)
	v_mfma_f32_16x16x32_f16 v[94:97], v[66:69], v[126:129], v[94:97]
	ds_read_b128 v[66:69], v139 offset:10240
	s_waitcnt lgkmcnt(7)
	v_mfma_f32_16x16x32_f16 v[98:101], v[70:73], v[126:129], v[98:101]
	ds_read_b128 v[70:73], v139 offset:11264
	s_waitcnt lgkmcnt(7)
	v_mfma_f32_16x16x32_f16 v[102:105], v[74:77], v[126:129], v[102:105]
	ds_read_b128 v[74:77], v139 offset:12288
	s_waitcnt lgkmcnt(7)
	v_mfma_f32_16x16x32_f16 v[106:109], v[78:81], v[126:129], v[106:109]
	ds_read_b128 v[78:81], v139 offset:13312
	s_waitcnt lgkmcnt(7)
	v_mfma_f32_16x16x32_f16 v[110:113], v[114:117], v[126:129], v[110:113]
	ds_read_b128 v[114:117], v139 offset:14336
	s_waitcnt lgkmcnt(6)
	v_mfma_f32_16x16x32_f16 v[82:85], v[118:121], v[130:133], v[82:85]
	ds_read_b128 v[118:121], v139 offset:15360
	s_waitcnt lgkmcnt(6)
	v_mfma_f32_16x16x32_f16 v[86:89], v[122:125], v[130:133], v[86:89]
	ds_read_b128 v[126:129], v137 offset:128
	ds_read_b128 v[122:125], v139 offset:16384
	s_waitcnt lgkmcnt(7)
	v_mfma_f32_16x16x32_f16 v[90:93], v[66:69], v[130:133], v[90:93]
	ds_read_b128 v[66:69], v139 offset:17408
	s_waitcnt lgkmcnt(7)
	v_mfma_f32_16x16x32_f16 v[94:97], v[70:73], v[130:133], v[94:97]
	ds_read_b128 v[70:73], v139 offset:18432
	s_waitcnt lgkmcnt(7)
	v_mfma_f32_16x16x32_f16 v[98:101], v[74:77], v[130:133], v[98:101]
	ds_read_b128 v[74:77], v139 offset:19456
	s_waitcnt lgkmcnt(7)
	v_mfma_f32_16x16x32_f16 v[102:105], v[78:81], v[130:133], v[102:105]
	ds_read_b128 v[78:81], v139 offset:20480
	s_waitcnt lgkmcnt(7)
	v_mfma_f32_16x16x32_f16 v[106:109], v[114:117], v[130:133], v[106:109]
	ds_read_b128 v[114:117], v139 offset:21504
	s_waitcnt lgkmcnt(7)
	v_mfma_f32_16x16x32_f16 v[110:113], v[118:121], v[130:133], v[110:113]
	ds_read_b128 v[118:121], v139 offset:22528
	s_waitcnt lgkmcnt(6)
	v_mfma_f32_16x16x32_f16 v[82:85], v[122:125], v[126:129], v[82:85]
	ds_read_b128 v[122:125], v139 offset:23552
	s_waitcnt lgkmcnt(6)
	v_mfma_f32_16x16x32_f16 v[86:89], v[66:69], v[126:129], v[86:89]
	ds_read_b128 v[130:133], v137 offset:192
	ds_read_b128 v[66:69], v139 offset:24576
	s_waitcnt lgkmcnt(7)
	v_mfma_f32_16x16x32_f16 v[90:93], v[70:73], v[126:129], v[90:93]
	ds_read_b128 v[70:73], v139 offset:25600
	s_waitcnt lgkmcnt(7)
	v_mfma_f32_16x16x32_f16 v[94:97], v[74:77], v[126:129], v[94:97]
	ds_read_b128 v[74:77], v139 offset:26624
	s_waitcnt lgkmcnt(7)
	v_mfma_f32_16x16x32_f16 v[98:101], v[78:81], v[126:129], v[98:101]
	ds_read_b128 v[78:81], v139 offset:27648
	s_waitcnt lgkmcnt(7)
	v_mfma_f32_16x16x32_f16 v[102:105], v[114:117], v[126:129], v[102:105]
	ds_read_b128 v[114:117], v139 offset:28672
	s_waitcnt lgkmcnt(7)
	v_mfma_f32_16x16x32_f16 v[106:109], v[118:121], v[126:129], v[106:109]
	ds_read_b128 v[118:121], v139 offset:29696
	s_waitcnt lgkmcnt(7)
	v_mfma_f32_16x16x32_f16 v[110:113], v[122:125], v[126:129], v[110:113]
	ds_read_b128 v[122:125], v139 offset:30720
	s_waitcnt lgkmcnt(6)
	v_mfma_f32_16x16x32_f16 v[82:85], v[66:69], v[130:133], v[82:85]
	ds_read_b128 v[66:69], v139 offset:31744
	s_waitcnt lgkmcnt(6)
	v_mfma_f32_16x16x32_f16 v[86:89], v[70:73], v[130:133], v[86:89]
	s_waitcnt lgkmcnt(5)
	v_mfma_f32_16x16x32_f16 v[90:93], v[74:77], v[130:133], v[90:93]
	s_waitcnt lgkmcnt(4)
	v_mfma_f32_16x16x32_f16 v[94:97], v[78:81], v[130:133], v[94:97]
	s_waitcnt lgkmcnt(3)
	v_mfma_f32_16x16x32_f16 v[98:101], v[114:117], v[130:133], v[98:101]
	s_waitcnt lgkmcnt(2)
	v_mfma_f32_16x16x32_f16 v[102:105], v[118:121], v[130:133], v[102:105]
	s_waitcnt lgkmcnt(1)
	v_mfma_f32_16x16x32_f16 v[106:109], v[122:125], v[130:133], v[106:109]
	s_waitcnt lgkmcnt(0)
	v_mfma_f32_16x16x32_f16 v[110:113], v[66:69], v[130:133], v[110:113]
	s_nop 7
	s_nop 3
	v_max_f32_e32 v82, 0, v82
	v_max_f32_e32 v83, 0, v83
	v_max_f32_e32 v84, 0, v84
	v_max_f32_e32 v85, 0, v85
	v_cvt_pk_f16_f32 v160, v82, v83
	v_cvt_pk_f16_f32 v161, v84, v85
	ds_write_b64 v140, v[160:161]
	v_max_f32_e32 v86, 0, v86
	v_max_f32_e32 v87, 0, v87
	v_max_f32_e32 v88, 0, v88
	v_max_f32_e32 v89, 0, v89
	v_cvt_pk_f16_f32 v162, v86, v87
	v_cvt_pk_f16_f32 v163, v88, v89
	ds_write_b64 v140, v[162:163] offset:32
	v_max_f32_e32 v90, 0, v90
	v_max_f32_e32 v91, 0, v91
	v_max_f32_e32 v92, 0, v92
	v_max_f32_e32 v93, 0, v93
	v_cvt_pk_f16_f32 v160, v90, v91
	v_cvt_pk_f16_f32 v161, v92, v93
	ds_write_b64 v140, v[160:161] offset:64
	v_max_f32_e32 v94, 0, v94
	v_max_f32_e32 v95, 0, v95
	v_max_f32_e32 v96, 0, v96
	v_max_f32_e32 v97, 0, v97
	v_cvt_pk_f16_f32 v162, v94, v95
	v_cvt_pk_f16_f32 v163, v96, v97
	ds_write_b64 v140, v[162:163] offset:96
	v_max_f32_e32 v98, 0, v98
	v_max_f32_e32 v99, 0, v99
	v_max_f32_e32 v100, 0, v100
	v_max_f32_e32 v101, 0, v101
	v_cvt_pk_f16_f32 v160, v98, v99
	v_cvt_pk_f16_f32 v161, v100, v101
	ds_write_b64 v140, v[160:161] offset:128
	v_max_f32_e32 v102, 0, v102
	v_max_f32_e32 v103, 0, v103
	v_max_f32_e32 v104, 0, v104
	v_max_f32_e32 v105, 0, v105
	v_cvt_pk_f16_f32 v162, v102, v103
	v_cvt_pk_f16_f32 v163, v104, v105
	ds_write_b64 v140, v[162:163] offset:160
	v_max_f32_e32 v106, 0, v106
	v_max_f32_e32 v107, 0, v107
	v_max_f32_e32 v108, 0, v108
	v_max_f32_e32 v109, 0, v109
	v_cvt_pk_f16_f32 v160, v106, v107
	v_cvt_pk_f16_f32 v161, v108, v109
	ds_write_b64 v140, v[160:161] offset:192
	v_max_f32_e32 v110, 0, v110
	v_max_f32_e32 v111, 0, v111
	v_max_f32_e32 v112, 0, v112
	v_max_f32_e32 v113, 0, v113
	v_cvt_pk_f16_f32 v162, v110, v111
	v_cvt_pk_f16_f32 v163, v112, v113
	ds_write_b64 v140, v[162:163] offset:224
	s_lshl_b32 s52, s33, 12
	v_add_u32_e32 v158, s52, v142
	ds_read_b128 v[114:117], v141
	ds_read_b128 v[118:121], v141 offset:1088
	ds_read_b128 v[122:125], v141 offset:2176
	ds_read_b128 v[126:129], v141 offset:3264
	s_waitcnt lgkmcnt(3)
	global_store_dwordx4 v158, v[114:117], s[22:23] sc1
	s_waitcnt lgkmcnt(2)
	global_store_dwordx4 v158, v[118:121], s[22:23] offset:1024 sc1
	s_waitcnt lgkmcnt(1)
	global_store_dwordx4 v158, v[122:125], s[22:23] offset:2048 sc1
	s_waitcnt lgkmcnt(0)
	global_store_dwordx4 v158, v[126:129], s[22:23] offset:3072 sc1
	s_nop 1
	s_mov_b32 s66, 0
	s_branch .Lfb_tilestart
